# epilogue de-serialisation: residual loads of all 4 batches hoisted to epilogue start in EpiBf16Res (ph5 layer1, ph8), one vmcnt(12) per batch
# speedup vs baseline: 1.0019x; 1.0019x over previous
; #define GAS __attribute__((address_space(1)))
; #define SB() __builtin_amdgcn_sched_barrier(0)
; __device__ __forceinline__ unsigned cvt_pk_bf16(float lo, float hi) { unsigned r; asm volatile("v_cvt_pk_bf16_f32 %0, %1, %2" : "=v"(r) : "v"(lo), "v"(hi)); return r; }
; __device__ __forceinline__ float bflo(unsigned w) { return __uint_as_float(w << 16); }
; __device__ __forceinline__ float bfhi(unsigned w) { return __uint_as_float(w & 0xffff0000u); }
;     __device__ __forceinline__ void operator()(const f32x4 (&acc)[2][2][4][2], const Unit& u, int wr, int wc, int fr, int fq) const {
;     ...
;           for (int mh = 0; mh < 4; mh += 2) { f32x4 rv[2][2][2]; u32x4 rw[2][2];
; #pragma unroll
;             for (int mm = 0; mm < 2; ++mm) { const size_t ro = (size_t)(ai * HALF + wr * 64 + (mh + mm) * 16 + fr) * u.ldc;
; #pragma unroll
;                 for (int bj = 0; bj < 2; ++bj) {
;                     if constexpr (RF32) { rv[mm][bj][0] = *(const GAS f32x4*)(rb + (ro + bj * HALF) * 4); rv[mm][bj][1] = *(const GAS f32x4*)(rb + (ro + bj * HALF + 4) * 4); }
;                     else rw[mm][bj] = *(const GAS u32x4*)(rb + (ro + bj * HALF) * 2); } }
;             SB();
; #pragma unroll
;             for (int mm = 0; mm < 2; ++mm) { const int m = mh + mm; const size_t ro = (size_t)(ai * HALF + wr * 64 + m * 16 + fr) * u.ldc;
; #pragma unroll
;                 for (int bj = 0; bj < 2; ++bj) { f32x4 r0, r1;
;                     if constexpr (RF32) { r0 = rv[mm][bj][0]; r1 = rv[mm][bj][1]; }
;                     else { const u32x4 q = rw[mm][bj]; r0 = f32x4{bflo(q.x), bfhi(q.x), bflo(q.y), bfhi(q.y)}; r1 = f32x4{bflo(q.z), bfhi(q.z), bflo(q.w), bfhi(q.w)}; }
;                     const f32x4 v0 = acc[ai][bj][m][0] + r0, v1 = acc[ai][bj][m][1] + r1;
;                     u32x4 w; w.x = cvt_pk_bf16(v0[0], v0[1]); w.y = cvt_pk_bf16(v0[2], v0[3]); w.z = cvt_pk_bf16(v1[0], v1[1]); w.w = cvt_pk_bf16(v1[2], v1[3]);
;                     *(u32x4*)(cb + ro + bj * HALF) = w; } }
;             SB(); } }
.LBB0_1088:
	v_mov_b32_e32 v148, v150
	v_lshl_add_u64 v[144:145], v[138:139], 0, s[46:47]
	v_add_u32_e32 v148, s33, v148
	v_and_b32_e32 v144, -2, v144
	v_ashrrev_i32_e32 v149, 31, v148
	v_lshl_add_u64 v[146:147], s[44:45], 0, v[144:145]
	v_lshlrev_b64 v[170:171], 12, v[148:149]
	v_lshl_add_u64 v[144:145], v[146:147], 0, v[170:171]
	global_load_dwordx4 v[154:157], v[144:145], off
	global_load_dwordx4 v[158:161], v[144:145], off offset:256
	v_add_u32_e32 v144, 16, v148
	v_ashrrev_i32_e32 v145, 31, v144
	v_lshlrev_b64 v[172:173], 12, v[144:145]
	v_lshl_add_u64 v[144:145], v[146:147], 0, v[172:173]
	global_load_dwordx4 v[162:165], v[144:145], off
	global_load_dwordx4 v[166:169], v[144:145], off offset:256
	s_nop 1
	v_add_u32_e32 v178, 32, v148
	v_add_u32_e32 v186, 48, v148
	v_ashrrev_i32_e32 v179, 31, v178
	v_ashrrev_i32_e32 v187, 31, v186
	v_lshlrev_b64 v[194:195], 12, v[178:179]
	v_lshlrev_b64 v[196:197], 12, v[186:187]
	v_lshl_add_u64 v[182:183], v[146:147], 0, v[194:195]
	v_lshl_add_u64 v[190:191], v[146:147], 0, v[196:197]
	global_load_dwordx4 v[178:181], v[182:183], off
	s_nop 0
	global_load_dwordx4 v[182:185], v[182:183], off offset:256
	s_nop 0
	global_load_dwordx4 v[186:189], v[190:191], off
	s_nop 0
	global_load_dwordx4 v[190:193], v[190:191], off offset:256
	s_nop 1
	v_add_u32_e32 v226, 0x80, v148
	v_add_u32_e32 v234, 0x90, v148
	v_ashrrev_i32_e32 v227, 31, v226
	v_ashrrev_i32_e32 v235, 31, v234
	v_lshlrev_b64 v[242:243], 12, v[226:227]
	v_lshlrev_b64 v[244:245], 12, v[234:235]
	v_lshl_add_u64 v[230:231], v[146:147], 0, v[242:243]
	v_lshl_add_u64 v[238:239], v[146:147], 0, v[244:245]
	global_load_dwordx4 v[226:229], v[230:231], off
	s_nop 0
	global_load_dwordx4 v[230:233], v[230:231], off offset:256
	s_nop 0
	global_load_dwordx4 v[234:237], v[238:239], off
	s_nop 0
	global_load_dwordx4 v[238:241], v[238:239], off offset:256
	s_nop 1
	v_add_u32_e32 v198, 0xa0, v148
	v_add_u32_e32 v206, 0xb0, v148
	v_ashrrev_i32_e32 v199, 31, v198
	v_ashrrev_i32_e32 v207, 31, v206
	v_lshlrev_b64 v[214:215], 12, v[198:199]
	v_lshlrev_b64 v[246:247], 12, v[206:207]
	v_lshl_add_u64 v[202:203], v[146:147], 0, v[214:215]
	v_lshl_add_u64 v[210:211], v[146:147], 0, v[246:247]
	global_load_dwordx4 v[198:201], v[202:203], off
	s_nop 0
	global_load_dwordx4 v[202:205], v[202:203], off offset:256
	s_nop 0
	global_load_dwordx4 v[206:209], v[210:211], off
	s_nop 0
	global_load_dwordx4 v[210:213], v[210:211], off offset:256
	s_add_u32 s14, s46, s79
	s_addc_u32 s15, s47, 0
	v_lshl_add_u64 v[144:145], v[136:137], 1, s[14:15]
	s_waitcnt vmcnt(12)
	v_lshlrev_b32_e32 v174, 16, v154
	v_and_b32_e32 v175, 0xffff0000, v154
	v_lshlrev_b32_e32 v154, 16, v155
	v_and_b32_e32 v155, 0xffff0000, v155
	v_lshlrev_b32_e32 v176, 16, v156
	v_and_b32_e32 v177, 0xffff0000, v156
	v_lshlrev_b32_e32 v156, 16, v157
	v_and_b32_e32 v157, 0xffff0000, v157
	v_lshl_add_u64 v[170:171], v[144:145], 0, v[170:171]
	v_pk_add_f32 v[128:129], v[128:129], v[154:155]
	v_pk_add_f32 v[126:127], v[126:127], v[174:175]
	v_pk_add_f32 v[154:155], v[124:125], v[156:157]
	v_pk_add_f32 v[124:125], v[122:123], v[176:177]
	v_cvt_pk_bf16_f32 v122, v126, v127
	v_cvt_pk_bf16_f32 v123, v128, v129
	v_lshlrev_b32_e32 v126, 16, v160
	v_cvt_pk_bf16_f32 v124, v124, v125
	v_cvt_pk_bf16_f32 v125, v154, v155
	global_store_dwordx4 v[170:171], v[122:125], off
	v_and_b32_e32 v127, 0xffff0000, v160
	v_lshlrev_b32_e32 v128, 16, v161
	v_lshlrev_b32_e32 v122, 16, v158
	v_and_b32_e32 v123, 0xffff0000, v158
	v_and_b32_e32 v129, 0xffff0000, v161
	v_lshlrev_b32_e32 v124, 16, v159
	v_and_b32_e32 v125, 0xffff0000, v159
	v_pk_add_f32 v[118:119], v[118:119], v[122:123]
	v_pk_add_f32 v[122:123], v[116:117], v[128:129]
	v_pk_add_f32 v[116:117], v[114:115], v[126:127]
	v_pk_add_f32 v[120:121], v[120:121], v[124:125]
	v_cvt_pk_bf16_f32 v114, v118, v119
	v_lshlrev_b32_e32 v118, 16, v163
	v_cvt_pk_bf16_f32 v115, v120, v121
	v_cvt_pk_bf16_f32 v116, v116, v117
	v_cvt_pk_bf16_f32 v117, v122, v123
	global_store_dwordx4 v[170:171], v[114:117], off offset:256
	v_and_b32_e32 v119, 0xffff0000, v163
	v_lshlrev_b32_e32 v120, 16, v164
	v_lshlrev_b32_e32 v116, 16, v162
	v_and_b32_e32 v117, 0xffff0000, v162
	v_and_b32_e32 v121, 0xffff0000, v164
	v_lshlrev_b32_e32 v122, 16, v165
	v_and_b32_e32 v123, 0xffff0000, v165
	v_lshl_add_u64 v[114:115], v[144:145], 0, v[172:173]
	v_pk_add_f32 v[112:113], v[112:113], v[118:119]
	v_pk_add_f32 v[110:111], v[110:111], v[116:117]
	v_pk_add_f32 v[116:117], v[108:109], v[122:123]
	v_pk_add_f32 v[108:109], v[106:107], v[120:121]
	v_cvt_pk_bf16_f32 v106, v110, v111
	v_cvt_pk_bf16_f32 v107, v112, v113
	v_lshlrev_b32_e32 v110, 16, v168
	v_cvt_pk_bf16_f32 v108, v108, v109
	v_cvt_pk_bf16_f32 v109, v116, v117
	global_store_dwordx4 v[114:115], v[106:109], off
	v_and_b32_e32 v111, 0xffff0000, v168
	v_lshlrev_b32_e32 v112, 16, v169
	v_lshlrev_b32_e32 v106, 16, v166
	v_and_b32_e32 v107, 0xffff0000, v166
	v_and_b32_e32 v113, 0xffff0000, v169
	v_lshlrev_b32_e32 v108, 16, v167
	v_and_b32_e32 v109, 0xffff0000, v167
	v_pk_add_f32 v[102:103], v[102:103], v[106:107]
	v_pk_add_f32 v[106:107], v[100:101], v[112:113]
	v_pk_add_f32 v[100:101], v[98:99], v[110:111]
	v_pk_add_f32 v[104:105], v[104:105], v[108:109]
	v_cvt_pk_bf16_f32 v98, v102, v103
	s_nop 0
	v_cvt_pk_bf16_f32 v99, v104, v105
	v_cvt_pk_bf16_f32 v100, v100, v101
	v_cvt_pk_bf16_f32 v101, v106, v107
	global_store_dwordx4 v[114:115], v[98:101], off offset:256
	s_waitcnt vmcnt(12)
; #define GAS __attribute__((address_space(1)))
; #define SB() __builtin_amdgcn_sched_barrier(0)
; __device__ __forceinline__ unsigned cvt_pk_bf16(float lo, float hi) { unsigned r; asm volatile("v_cvt_pk_bf16_f32 %0, %1, %2" : "=v"(r) : "v"(lo), "v"(hi)); return r; }
; __device__ __forceinline__ float bflo(unsigned w) { return __uint_as_float(w << 16); }
; __device__ __forceinline__ float bfhi(unsigned w) { return __uint_as_float(w & 0xffff0000u); }
;     __device__ __forceinline__ void operator()(const f32x4 (&acc)[2][2][4][2], const Unit& u, int wr, int wc, int fr, int fq) const {
;     ...
;           for (int mh = 0; mh < 4; mh += 2) { f32x4 rv[2][2][2]; u32x4 rw[2][2];
; #pragma unroll
;             for (int mm = 0; mm < 2; ++mm) { const size_t ro = (size_t)(ai * HALF + wr * 64 + (mh + mm) * 16 + fr) * u.ldc;
; #pragma unroll
;                 for (int bj = 0; bj < 2; ++bj) {
;                     if constexpr (RF32) { rv[mm][bj][0] = *(const GAS f32x4*)(rb + (ro + bj * HALF) * 4); rv[mm][bj][1] = *(const GAS f32x4*)(rb + (ro + bj * HALF + 4) * 4); }
;                     else rw[mm][bj] = *(const GAS u32x4*)(rb + (ro + bj * HALF) * 2); } }
;             SB();
; #pragma unroll
;             for (int mm = 0; mm < 2; ++mm) { const int m = mh + mm; const size_t ro = (size_t)(ai * HALF + wr * 64 + m * 16 + fr) * u.ldc;
; #pragma unroll
;                 for (int bj = 0; bj < 2; ++bj) { f32x4 r0, r1;
;                     if constexpr (RF32) { r0 = rv[mm][bj][0]; r1 = rv[mm][bj][1]; }
;                     else { const u32x4 q = rw[mm][bj]; r0 = f32x4{bflo(q.x), bfhi(q.x), bflo(q.y), bfhi(q.y)}; r1 = f32x4{bflo(q.z), bfhi(q.z), bflo(q.w), bfhi(q.w)}; }
;                     const f32x4 v0 = acc[ai][bj][m][0] + r0, v1 = acc[ai][bj][m][1] + r1;
;                     u32x4 w; w.x = cvt_pk_bf16(v0[0], v0[1]); w.y = cvt_pk_bf16(v0[2], v0[3]); w.z = cvt_pk_bf16(v1[0], v1[1]); w.w = cvt_pk_bf16(v1[2], v1[3]);
;                     *(u32x4*)(cb + ro + bj * HALF) = w; } }
;             SB(); } }
	v_lshlrev_b32_e32 v118, 16, v178
	v_and_b32_e32 v119, 0xffff0000, v178
	v_lshlrev_b32_e32 v178, 16, v179
	v_and_b32_e32 v179, 0xffff0000, v179
	v_lshlrev_b32_e32 v120, 16, v180
	v_and_b32_e32 v121, 0xffff0000, v180
	v_lshlrev_b32_e32 v180, 16, v181
	v_and_b32_e32 v181, 0xffff0000, v181
	v_lshl_add_u64 v[194:195], v[144:145], 0, v[194:195]
	v_pk_add_f32 v[96:97], v[96:97], v[178:179]
	v_pk_add_f32 v[94:95], v[94:95], v[118:119]
	v_pk_add_f32 v[178:179], v[92:93], v[180:181]
	v_pk_add_f32 v[92:93], v[90:91], v[120:121]
	v_cvt_pk_bf16_f32 v90, v94, v95
	v_cvt_pk_bf16_f32 v91, v96, v97
	v_lshlrev_b32_e32 v94, 16, v184
	v_cvt_pk_bf16_f32 v92, v92, v93
	v_cvt_pk_bf16_f32 v93, v178, v179
	global_store_dwordx4 v[194:195], v[90:93], off
	v_and_b32_e32 v95, 0xffff0000, v184
	v_lshlrev_b32_e32 v96, 16, v185
	v_lshlrev_b32_e32 v90, 16, v182
	v_and_b32_e32 v91, 0xffff0000, v182
	v_and_b32_e32 v97, 0xffff0000, v185
	v_lshlrev_b32_e32 v92, 16, v183
	v_and_b32_e32 v93, 0xffff0000, v183
	v_pk_add_f32 v[86:87], v[86:87], v[90:91]
	v_pk_add_f32 v[90:91], v[84:85], v[96:97]
	v_pk_add_f32 v[84:85], v[82:83], v[94:95]
	v_pk_add_f32 v[88:89], v[88:89], v[92:93]
	v_cvt_pk_bf16_f32 v82, v86, v87
	v_lshlrev_b32_e32 v86, 16, v187
	v_cvt_pk_bf16_f32 v83, v88, v89
	v_cvt_pk_bf16_f32 v84, v84, v85
	v_cvt_pk_bf16_f32 v85, v90, v91
	global_store_dwordx4 v[194:195], v[82:85], off offset:256
	v_and_b32_e32 v87, 0xffff0000, v187
	v_lshlrev_b32_e32 v88, 16, v188
	v_lshlrev_b32_e32 v84, 16, v186
	v_and_b32_e32 v85, 0xffff0000, v186
	v_and_b32_e32 v89, 0xffff0000, v188
	v_lshlrev_b32_e32 v90, 16, v189
	v_and_b32_e32 v91, 0xffff0000, v189
	v_lshl_add_u64 v[82:83], v[144:145], 0, v[196:197]
	v_pk_add_f32 v[80:81], v[80:81], v[86:87]
	v_pk_add_f32 v[78:79], v[78:79], v[84:85]
	v_pk_add_f32 v[84:85], v[76:77], v[90:91]
	v_pk_add_f32 v[76:77], v[74:75], v[88:89]
	v_cvt_pk_bf16_f32 v74, v78, v79
	v_cvt_pk_bf16_f32 v75, v80, v81
	v_lshlrev_b32_e32 v78, 16, v192
	v_cvt_pk_bf16_f32 v76, v76, v77
	v_cvt_pk_bf16_f32 v77, v84, v85
	global_store_dwordx4 v[82:83], v[74:77], off
	v_and_b32_e32 v79, 0xffff0000, v192
	v_lshlrev_b32_e32 v80, 16, v193
	v_lshlrev_b32_e32 v74, 16, v190
	v_and_b32_e32 v75, 0xffff0000, v190
	v_and_b32_e32 v81, 0xffff0000, v193
	v_lshlrev_b32_e32 v76, 16, v191
	v_and_b32_e32 v77, 0xffff0000, v191
	v_pk_add_f32 v[70:71], v[70:71], v[74:75]
	v_pk_add_f32 v[74:75], v[68:69], v[80:81]
	v_pk_add_f32 v[68:69], v[66:67], v[78:79]
	v_pk_add_f32 v[72:73], v[72:73], v[76:77]
	v_cvt_pk_bf16_f32 v66, v70, v71
	s_nop 0
	v_cvt_pk_bf16_f32 v67, v72, v73
	v_cvt_pk_bf16_f32 v68, v68, v69
	v_cvt_pk_bf16_f32 v69, v74, v75
	global_store_dwordx4 v[82:83], v[66:69], off offset:256
	s_waitcnt vmcnt(12)
	v_lshlrev_b32_e32 v86, 16, v226
	v_and_b32_e32 v87, 0xffff0000, v226
	v_lshlrev_b32_e32 v226, 16, v227
	v_and_b32_e32 v227, 0xffff0000, v227
	v_lshlrev_b32_e32 v88, 16, v228
	v_and_b32_e32 v89, 0xffff0000, v228
	v_lshlrev_b32_e32 v228, 16, v229
	v_and_b32_e32 v229, 0xffff0000, v229
	v_lshl_add_u64 v[242:243], v[144:145], 0, v[242:243]
	v_pk_add_f32 v[64:65], v[64:65], v[226:227]
	v_pk_add_f32 v[62:63], v[62:63], v[86:87]
	v_pk_add_f32 v[226:227], v[60:61], v[228:229]
	v_pk_add_f32 v[60:61], v[58:59], v[88:89]
	v_cvt_pk_bf16_f32 v58, v62, v63
	v_cvt_pk_bf16_f32 v59, v64, v65
	v_lshlrev_b32_e32 v62, 16, v232
	v_cvt_pk_bf16_f32 v60, v60, v61
	v_cvt_pk_bf16_f32 v61, v226, v227
	global_store_dwordx4 v[242:243], v[58:61], off
	v_and_b32_e32 v63, 0xffff0000, v232
	v_lshlrev_b32_e32 v64, 16, v233
	v_lshlrev_b32_e32 v58, 16, v230
	v_and_b32_e32 v59, 0xffff0000, v230
	v_and_b32_e32 v65, 0xffff0000, v233
	v_lshlrev_b32_e32 v60, 16, v231
	v_and_b32_e32 v61, 0xffff0000, v231
	v_pk_add_f32 v[54:55], v[54:55], v[58:59]
	v_pk_add_f32 v[58:59], v[52:53], v[64:65]
	v_pk_add_f32 v[52:53], v[50:51], v[62:63]
	v_pk_add_f32 v[56:57], v[56:57], v[60:61]
	v_cvt_pk_bf16_f32 v50, v54, v55
	v_lshlrev_b32_e32 v54, 16, v235
	v_cvt_pk_bf16_f32 v51, v56, v57
	v_cvt_pk_bf16_f32 v52, v52, v53
	v_cvt_pk_bf16_f32 v53, v58, v59
	global_store_dwordx4 v[242:243], v[50:53], off offset:256
	v_and_b32_e32 v55, 0xffff0000, v235
	v_lshlrev_b32_e32 v56, 16, v236
	v_lshlrev_b32_e32 v52, 16, v234
	v_and_b32_e32 v53, 0xffff0000, v234
	v_and_b32_e32 v57, 0xffff0000, v236
	v_lshlrev_b32_e32 v58, 16, v237
	v_and_b32_e32 v59, 0xffff0000, v237
	v_lshl_add_u64 v[50:51], v[144:145], 0, v[244:245]
	v_pk_add_f32 v[48:49], v[48:49], v[54:55]
	v_pk_add_f32 v[46:47], v[46:47], v[52:53]
	v_pk_add_f32 v[52:53], v[44:45], v[58:59]
	v_pk_add_f32 v[44:45], v[42:43], v[56:57]
	v_cvt_pk_bf16_f32 v42, v46, v47
	v_cvt_pk_bf16_f32 v43, v48, v49
	v_lshlrev_b32_e32 v46, 16, v240
	v_cvt_pk_bf16_f32 v44, v44, v45
	v_cvt_pk_bf16_f32 v45, v52, v53
	global_store_dwordx4 v[50:51], v[42:45], off
	v_and_b32_e32 v47, 0xffff0000, v240
	v_lshlrev_b32_e32 v48, 16, v241
	v_lshlrev_b32_e32 v42, 16, v238
	v_and_b32_e32 v43, 0xffff0000, v238
	v_and_b32_e32 v49, 0xffff0000, v241
	v_lshlrev_b32_e32 v44, 16, v239
	v_and_b32_e32 v45, 0xffff0000, v239
	v_pk_add_f32 v[38:39], v[38:39], v[42:43]
	v_pk_add_f32 v[42:43], v[36:37], v[48:49]
	v_pk_add_f32 v[36:37], v[34:35], v[46:47]
	v_pk_add_f32 v[40:41], v[40:41], v[44:45]
	v_cvt_pk_bf16_f32 v34, v38, v39
	s_nop 0
	v_cvt_pk_bf16_f32 v35, v40, v41
	v_cvt_pk_bf16_f32 v36, v36, v37
	v_cvt_pk_bf16_f32 v37, v42, v43
	global_store_dwordx4 v[50:51], v[34:37], off offset:256
	s_waitcnt vmcnt(12)
; #define SB() __builtin_amdgcn_sched_barrier(0)
; __device__ __forceinline__ unsigned cvt_pk_bf16(float lo, float hi) { unsigned r; asm volatile("v_cvt_pk_bf16_f32 %0, %1, %2" : "=v"(r) : "v"(lo), "v"(hi)); return r; }
; __device__ __forceinline__ float bflo(unsigned w) { return __uint_as_float(w << 16); }
; __device__ __forceinline__ float bfhi(unsigned w) { return __uint_as_float(w & 0xffff0000u); }
; #define PG8_BAR __builtin_amdgcn_s_barrier()
;     ...
;         if (!has_next) break;
; #pragma unroll
;         for (int a = 0; a < 2; ++a)
; #pragma unroll
;             for (int b = 0; b < 2; ++b)
; #pragma unroll
;                 for (int m = 0; m < 4; ++m)
; #pragma unroll
;                     for (int n = 0; n < 2; ++n) acc[a][b][m][n] = (f32x4){0.f, 0.f, 0.f, 0.f};
;         cur = nxt; cA = nA; cB = nB; ++ui; nt = PG8_NT(cur);
;         if constexpr (GATHER) { cg[0] = ng[0]; cg[1] = ng[1]; }
;         if constexpr (ALIGN_EPI) { if (wr == 1) PG8_BAR; }
;     __device__ __forceinline__ void operator()(const f32x4 (&acc)[2][2][4][2], const Unit& u, int wr, int wc, int fr, int fq) const {
;     ...
;             for (int mm = 0; mm < 2; ++mm) { const int m = mh + mm; const size_t ro = (size_t)(ai * HALF + wr * 64 + m * 16 + fr) * u.ldc;
; #pragma unroll
;                 for (int bj = 0; bj < 2; ++bj) { f32x4 r0, r1;
;                     if constexpr (RF32) { r0 = rv[mm][bj][0]; r1 = rv[mm][bj][1]; }
;                     else { const u32x4 q = rw[mm][bj]; r0 = f32x4{bflo(q.x), bfhi(q.x), bflo(q.y), bfhi(q.y)}; r1 = f32x4{bflo(q.z), bfhi(q.z), bflo(q.w), bfhi(q.w)}; }
;                     const f32x4 v0 = acc[ai][bj][m][0] + r0, v1 = acc[ai][bj][m][1] + r1;
;                     u32x4 w; w.x = cvt_pk_bf16(v0[0], v0[1]); w.y = cvt_pk_bf16(v0[2], v0[3]); w.z = cvt_pk_bf16(v1[0], v1[1]); w.w = cvt_pk_bf16(v1[2], v1[3]);
;                     *(u32x4*)(cb + ro + bj * HALF) = w; } }
;             SB(); } }
	v_lshlrev_b32_e32 v54, 16, v198
	v_and_b32_e32 v55, 0xffff0000, v198
	v_lshlrev_b32_e32 v198, 16, v199
	v_and_b32_e32 v199, 0xffff0000, v199
	v_lshlrev_b32_e32 v56, 16, v200
	v_and_b32_e32 v57, 0xffff0000, v200
	v_lshlrev_b32_e32 v200, 16, v201
	v_and_b32_e32 v201, 0xffff0000, v201
	v_lshl_add_u64 v[214:215], v[144:145], 0, v[214:215]
	v_pk_add_f32 v[32:33], v[32:33], v[198:199]
	v_pk_add_f32 v[30:31], v[30:31], v[54:55]
	v_pk_add_f32 v[198:199], v[28:29], v[200:201]
	v_pk_add_f32 v[28:29], v[26:27], v[56:57]
	v_cvt_pk_bf16_f32 v26, v30, v31
	v_cvt_pk_bf16_f32 v27, v32, v33
	v_lshlrev_b32_e32 v30, 16, v204
	v_cvt_pk_bf16_f32 v28, v28, v29
	v_cvt_pk_bf16_f32 v29, v198, v199
	global_store_dwordx4 v[214:215], v[26:29], off
	v_and_b32_e32 v31, 0xffff0000, v204
	v_lshlrev_b32_e32 v32, 16, v205
	v_lshlrev_b32_e32 v26, 16, v202
	v_and_b32_e32 v27, 0xffff0000, v202
	v_and_b32_e32 v33, 0xffff0000, v205
	v_lshlrev_b32_e32 v28, 16, v203
	v_and_b32_e32 v29, 0xffff0000, v203
	v_pk_add_f32 v[22:23], v[22:23], v[26:27]
	v_pk_add_f32 v[26:27], v[20:21], v[32:33]
	v_pk_add_f32 v[20:21], v[18:19], v[30:31]
	v_pk_add_f32 v[24:25], v[24:25], v[28:29]
	v_cvt_pk_bf16_f32 v18, v22, v23
	v_lshlrev_b32_e32 v22, 16, v207
	v_cvt_pk_bf16_f32 v19, v24, v25
	v_cvt_pk_bf16_f32 v20, v20, v21
	v_cvt_pk_bf16_f32 v21, v26, v27
	global_store_dwordx4 v[214:215], v[18:21], off offset:256
	v_and_b32_e32 v23, 0xffff0000, v207
	v_lshlrev_b32_e32 v24, 16, v208
	v_lshlrev_b32_e32 v20, 16, v206
	v_and_b32_e32 v21, 0xffff0000, v206
	v_and_b32_e32 v25, 0xffff0000, v208
	v_lshlrev_b32_e32 v26, 16, v209
	v_and_b32_e32 v27, 0xffff0000, v209
	v_lshl_add_u64 v[18:19], v[144:145], 0, v[246:247]
	v_pk_add_f32 v[16:17], v[16:17], v[22:23]
	v_pk_add_f32 v[14:15], v[14:15], v[20:21]
	v_pk_add_f32 v[20:21], v[12:13], v[26:27]
	v_pk_add_f32 v[12:13], v[10:11], v[24:25]
	v_cvt_pk_bf16_f32 v10, v14, v15
	v_cvt_pk_bf16_f32 v11, v16, v17
	v_lshlrev_b32_e32 v14, 16, v212
	v_cvt_pk_bf16_f32 v12, v12, v13
	v_cvt_pk_bf16_f32 v13, v20, v21
	global_store_dwordx4 v[18:19], v[10:13], off
	v_and_b32_e32 v15, 0xffff0000, v212
	v_lshlrev_b32_e32 v16, 16, v213
	v_lshlrev_b32_e32 v10, 16, v210
	v_and_b32_e32 v11, 0xffff0000, v210
	v_and_b32_e32 v17, 0xffff0000, v213
	v_lshlrev_b32_e32 v12, 16, v211
	v_and_b32_e32 v13, 0xffff0000, v211
	v_pk_add_f32 v[6:7], v[6:7], v[10:11]
	v_pk_add_f32 v[10:11], v[4:5], v[16:17]
	v_pk_add_f32 v[4:5], v[2:3], v[14:15]
	v_pk_add_f32 v[8:9], v[8:9], v[12:13]
	v_cvt_pk_bf16_f32 v2, v6, v7
	s_nop 0
	v_cvt_pk_bf16_f32 v3, v8, v9
	v_cvt_pk_bf16_f32 v4, v4, v5
	v_cvt_pk_bf16_f32 v5, v10, v11
	global_store_dwordx4 v[18:19], v[2:5], off offset:256
	v_readlane_b32 s18, v248, 9
	v_readlane_b32 s16, v248, 11
	s_and_b64 vcc, exec, s[58:59]
	s_mov_b64 s[46:47], -1
	v_readlane_b32 s19, v248, 10
	v_readlane_b32 s17, v248, 12
	s_cbranch_vccnz .LBB0_1073
	s_and_b64 vcc, exec, s[56:57]
	s_cbranch_vccnz .LBB0_1072
	s_barrier
	s_branch .LBB0_1072

; #define GAS __attribute__((address_space(1)))
; #define SB() __builtin_amdgcn_sched_barrier(0)
; __device__ __forceinline__ unsigned cvt_pk_bf16(float lo, float hi) { unsigned r; asm volatile("v_cvt_pk_bf16_f32 %0, %1, %2" : "=v"(r) : "v"(lo), "v"(hi)); return r; }
; __device__ __forceinline__ float bflo(unsigned w) { return __uint_as_float(w << 16); }
; __device__ __forceinline__ float bfhi(unsigned w) { return __uint_as_float(w & 0xffff0000u); }
;     __device__ __forceinline__ void operator()(const f32x4 (&acc)[2][2][4][2], const Unit& u, int wr, int wc, int fr, int fq) const {
;     ...
;           for (int mh = 0; mh < 4; mh += 2) { f32x4 rv[2][2][2]; u32x4 rw[2][2];
; #pragma unroll
;             for (int mm = 0; mm < 2; ++mm) { const size_t ro = (size_t)(ai * HALF + wr * 64 + (mh + mm) * 16 + fr) * u.ldc;
; #pragma unroll
;                 for (int bj = 0; bj < 2; ++bj) {
;                     if constexpr (RF32) { rv[mm][bj][0] = *(const GAS f32x4*)(rb + (ro + bj * HALF) * 4); rv[mm][bj][1] = *(const GAS f32x4*)(rb + (ro + bj * HALF + 4) * 4); }
;                     else rw[mm][bj] = *(const GAS u32x4*)(rb + (ro + bj * HALF) * 2); } }
;             SB();
; #pragma unroll
;             for (int mm = 0; mm < 2; ++mm) { const int m = mh + mm; const size_t ro = (size_t)(ai * HALF + wr * 64 + m * 16 + fr) * u.ldc;
; #pragma unroll
;                 for (int bj = 0; bj < 2; ++bj) { f32x4 r0, r1;
;                     if constexpr (RF32) { r0 = rv[mm][bj][0]; r1 = rv[mm][bj][1]; }
;                     else { const u32x4 q = rw[mm][bj]; r0 = f32x4{bflo(q.x), bfhi(q.x), bflo(q.y), bfhi(q.y)}; r1 = f32x4{bflo(q.z), bfhi(q.z), bflo(q.w), bfhi(q.w)}; }
;                     const f32x4 v0 = acc[ai][bj][m][0] + r0, v1 = acc[ai][bj][m][1] + r1;
;                     u32x4 w; w.x = cvt_pk_bf16(v0[0], v0[1]); w.y = cvt_pk_bf16(v0[2], v0[3]); w.z = cvt_pk_bf16(v1[0], v1[1]); w.w = cvt_pk_bf16(v1[2], v1[3]);
;                     *(u32x4*)(cb + ro + bj * HALF) = w; } }
;             SB(); } }
.LBB0_1395:
	v_mov_b32_e32 v148, v150
	v_lshl_add_u64 v[144:145], v[138:139], 0, s[46:47]
	v_add_u32_e32 v148, s33, v148
	v_and_b32_e32 v144, -2, v144
	v_ashrrev_i32_e32 v149, 31, v148
	v_lshl_add_u64 v[146:147], s[4:5], 0, v[144:145]
	v_lshlrev_b64 v[170:171], 12, v[148:149]
	v_lshl_add_u64 v[144:145], v[146:147], 0, v[170:171]
	global_load_dwordx4 v[154:157], v[144:145], off
	global_load_dwordx4 v[158:161], v[144:145], off offset:256
	v_add_u32_e32 v144, 16, v148
	v_ashrrev_i32_e32 v145, 31, v144
	v_lshlrev_b64 v[172:173], 12, v[144:145]
	v_lshl_add_u64 v[144:145], v[146:147], 0, v[172:173]
	global_load_dwordx4 v[162:165], v[144:145], off
	global_load_dwordx4 v[166:169], v[144:145], off offset:256
	s_nop 1
	v_add_u32_e32 v178, 32, v148
	v_add_u32_e32 v186, 48, v148
	v_ashrrev_i32_e32 v179, 31, v178
	v_ashrrev_i32_e32 v187, 31, v186
	v_lshlrev_b64 v[194:195], 12, v[178:179]
	v_lshlrev_b64 v[196:197], 12, v[186:187]
	v_lshl_add_u64 v[182:183], v[146:147], 0, v[194:195]
	v_lshl_add_u64 v[190:191], v[146:147], 0, v[196:197]
	global_load_dwordx4 v[178:181], v[182:183], off
	s_nop 0
	global_load_dwordx4 v[182:185], v[182:183], off offset:256
	s_nop 0
	global_load_dwordx4 v[186:189], v[190:191], off
	s_nop 0
	global_load_dwordx4 v[190:193], v[190:191], off offset:256
	s_nop 1
	v_add_u32_e32 v226, 0x80, v148
	v_add_u32_e32 v234, 0x90, v148
	v_ashrrev_i32_e32 v227, 31, v226
	v_ashrrev_i32_e32 v235, 31, v234
	v_lshlrev_b64 v[242:243], 12, v[226:227]
	v_lshlrev_b64 v[244:245], 12, v[234:235]
	v_lshl_add_u64 v[230:231], v[146:147], 0, v[242:243]
	v_lshl_add_u64 v[238:239], v[146:147], 0, v[244:245]
	global_load_dwordx4 v[226:229], v[230:231], off
	s_nop 0
	global_load_dwordx4 v[230:233], v[230:231], off offset:256
	s_nop 0
	global_load_dwordx4 v[234:237], v[238:239], off
	s_nop 0
	global_load_dwordx4 v[238:241], v[238:239], off offset:256
	s_nop 1
	v_add_u32_e32 v198, 0xa0, v148
	v_add_u32_e32 v206, 0xb0, v148
	v_ashrrev_i32_e32 v199, 31, v198
	v_ashrrev_i32_e32 v207, 31, v206
	v_lshlrev_b64 v[214:215], 12, v[198:199]
	v_lshlrev_b64 v[246:247], 12, v[206:207]
	v_lshl_add_u64 v[202:203], v[146:147], 0, v[214:215]
	v_lshl_add_u64 v[210:211], v[146:147], 0, v[246:247]
	global_load_dwordx4 v[198:201], v[202:203], off
	s_nop 0
	global_load_dwordx4 v[202:205], v[202:203], off offset:256
	s_nop 0
	global_load_dwordx4 v[206:209], v[210:211], off
	s_nop 0
	global_load_dwordx4 v[210:213], v[210:211], off offset:256
	s_add_u32 s18, s46, s79
	s_addc_u32 s19, s47, 0
	v_lshl_add_u64 v[144:145], v[136:137], 1, s[18:19]
	s_waitcnt vmcnt(12)
	v_lshlrev_b32_e32 v174, 16, v154
	v_and_b32_e32 v175, 0xffff0000, v154
	v_lshlrev_b32_e32 v154, 16, v155
	v_and_b32_e32 v155, 0xffff0000, v155
	v_lshlrev_b32_e32 v176, 16, v156
	v_and_b32_e32 v177, 0xffff0000, v156
	v_lshlrev_b32_e32 v156, 16, v157
	v_and_b32_e32 v157, 0xffff0000, v157
	v_lshl_add_u64 v[170:171], v[144:145], 0, v[170:171]
	v_pk_add_f32 v[128:129], v[128:129], v[154:155]
	v_pk_add_f32 v[126:127], v[126:127], v[174:175]
	v_pk_add_f32 v[154:155], v[124:125], v[156:157]
	v_pk_add_f32 v[124:125], v[122:123], v[176:177]
	v_cvt_pk_bf16_f32 v122, v126, v127
	v_cvt_pk_bf16_f32 v123, v128, v129
	v_lshlrev_b32_e32 v126, 16, v160
	v_cvt_pk_bf16_f32 v124, v124, v125
	v_cvt_pk_bf16_f32 v125, v154, v155
	global_store_dwordx4 v[170:171], v[122:125], off
	v_and_b32_e32 v127, 0xffff0000, v160
	v_lshlrev_b32_e32 v128, 16, v161
	v_lshlrev_b32_e32 v122, 16, v158
	v_and_b32_e32 v123, 0xffff0000, v158
	v_and_b32_e32 v129, 0xffff0000, v161
	v_lshlrev_b32_e32 v124, 16, v159
	v_and_b32_e32 v125, 0xffff0000, v159
	v_pk_add_f32 v[118:119], v[118:119], v[122:123]
	v_pk_add_f32 v[122:123], v[116:117], v[128:129]
	v_pk_add_f32 v[116:117], v[114:115], v[126:127]
	v_pk_add_f32 v[120:121], v[120:121], v[124:125]
	v_cvt_pk_bf16_f32 v114, v118, v119
	v_lshlrev_b32_e32 v118, 16, v163
	v_cvt_pk_bf16_f32 v115, v120, v121
	v_cvt_pk_bf16_f32 v116, v116, v117
	v_cvt_pk_bf16_f32 v117, v122, v123
	global_store_dwordx4 v[170:171], v[114:117], off offset:256
	v_and_b32_e32 v119, 0xffff0000, v163
	v_lshlrev_b32_e32 v120, 16, v164
	v_lshlrev_b32_e32 v116, 16, v162
	v_and_b32_e32 v117, 0xffff0000, v162
	v_and_b32_e32 v121, 0xffff0000, v164
	v_lshlrev_b32_e32 v122, 16, v165
	v_and_b32_e32 v123, 0xffff0000, v165
	v_lshl_add_u64 v[114:115], v[144:145], 0, v[172:173]
	v_pk_add_f32 v[112:113], v[112:113], v[118:119]
	v_pk_add_f32 v[110:111], v[110:111], v[116:117]
	v_pk_add_f32 v[116:117], v[108:109], v[122:123]
	v_pk_add_f32 v[108:109], v[106:107], v[120:121]
	v_cvt_pk_bf16_f32 v106, v110, v111
	v_cvt_pk_bf16_f32 v107, v112, v113
	v_lshlrev_b32_e32 v110, 16, v168
	v_cvt_pk_bf16_f32 v108, v108, v109
	v_cvt_pk_bf16_f32 v109, v116, v117
	global_store_dwordx4 v[114:115], v[106:109], off
	v_and_b32_e32 v111, 0xffff0000, v168
	v_lshlrev_b32_e32 v112, 16, v169
	v_lshlrev_b32_e32 v106, 16, v166
	v_and_b32_e32 v107, 0xffff0000, v166
	v_and_b32_e32 v113, 0xffff0000, v169
	v_lshlrev_b32_e32 v108, 16, v167
	v_and_b32_e32 v109, 0xffff0000, v167
	v_pk_add_f32 v[102:103], v[102:103], v[106:107]
	v_pk_add_f32 v[106:107], v[100:101], v[112:113]
	v_pk_add_f32 v[100:101], v[98:99], v[110:111]
	v_pk_add_f32 v[104:105], v[104:105], v[108:109]
	v_cvt_pk_bf16_f32 v98, v102, v103
	s_nop 0
	v_cvt_pk_bf16_f32 v99, v104, v105
	v_cvt_pk_bf16_f32 v100, v100, v101
	v_cvt_pk_bf16_f32 v101, v106, v107
	global_store_dwordx4 v[114:115], v[98:101], off offset:256
	s_waitcnt vmcnt(12)
; #define GAS __attribute__((address_space(1)))
; #define SB() __builtin_amdgcn_sched_barrier(0)
; __device__ __forceinline__ unsigned cvt_pk_bf16(float lo, float hi) { unsigned r; asm volatile("v_cvt_pk_bf16_f32 %0, %1, %2" : "=v"(r) : "v"(lo), "v"(hi)); return r; }
; __device__ __forceinline__ float bflo(unsigned w) { return __uint_as_float(w << 16); }
; __device__ __forceinline__ float bfhi(unsigned w) { return __uint_as_float(w & 0xffff0000u); }
;     __device__ __forceinline__ void operator()(const f32x4 (&acc)[2][2][4][2], const Unit& u, int wr, int wc, int fr, int fq) const {
;     ...
;           for (int mh = 0; mh < 4; mh += 2) { f32x4 rv[2][2][2]; u32x4 rw[2][2];
; #pragma unroll
;             for (int mm = 0; mm < 2; ++mm) { const size_t ro = (size_t)(ai * HALF + wr * 64 + (mh + mm) * 16 + fr) * u.ldc;
; #pragma unroll
;                 for (int bj = 0; bj < 2; ++bj) {
;                     if constexpr (RF32) { rv[mm][bj][0] = *(const GAS f32x4*)(rb + (ro + bj * HALF) * 4); rv[mm][bj][1] = *(const GAS f32x4*)(rb + (ro + bj * HALF + 4) * 4); }
;                     else rw[mm][bj] = *(const GAS u32x4*)(rb + (ro + bj * HALF) * 2); } }
;             SB();
; #pragma unroll
;             for (int mm = 0; mm < 2; ++mm) { const int m = mh + mm; const size_t ro = (size_t)(ai * HALF + wr * 64 + m * 16 + fr) * u.ldc;
; #pragma unroll
;                 for (int bj = 0; bj < 2; ++bj) { f32x4 r0, r1;
;                     if constexpr (RF32) { r0 = rv[mm][bj][0]; r1 = rv[mm][bj][1]; }
;                     else { const u32x4 q = rw[mm][bj]; r0 = f32x4{bflo(q.x), bfhi(q.x), bflo(q.y), bfhi(q.y)}; r1 = f32x4{bflo(q.z), bfhi(q.z), bflo(q.w), bfhi(q.w)}; }
;                     const f32x4 v0 = acc[ai][bj][m][0] + r0, v1 = acc[ai][bj][m][1] + r1;
;                     u32x4 w; w.x = cvt_pk_bf16(v0[0], v0[1]); w.y = cvt_pk_bf16(v0[2], v0[3]); w.z = cvt_pk_bf16(v1[0], v1[1]); w.w = cvt_pk_bf16(v1[2], v1[3]);
;                     *(u32x4*)(cb + ro + bj * HALF) = w; } }
;             SB(); } }
	v_lshlrev_b32_e32 v118, 16, v178
	v_and_b32_e32 v119, 0xffff0000, v178
	v_lshlrev_b32_e32 v178, 16, v179
	v_and_b32_e32 v179, 0xffff0000, v179
	v_lshlrev_b32_e32 v120, 16, v180
	v_and_b32_e32 v121, 0xffff0000, v180
	v_lshlrev_b32_e32 v180, 16, v181
	v_and_b32_e32 v181, 0xffff0000, v181
	v_lshl_add_u64 v[194:195], v[144:145], 0, v[194:195]
	v_pk_add_f32 v[96:97], v[96:97], v[178:179]
	v_pk_add_f32 v[94:95], v[94:95], v[118:119]
	v_pk_add_f32 v[178:179], v[92:93], v[180:181]
	v_pk_add_f32 v[92:93], v[90:91], v[120:121]
	v_cvt_pk_bf16_f32 v90, v94, v95
	v_cvt_pk_bf16_f32 v91, v96, v97
	v_lshlrev_b32_e32 v94, 16, v184
	v_cvt_pk_bf16_f32 v92, v92, v93
	v_cvt_pk_bf16_f32 v93, v178, v179
	global_store_dwordx4 v[194:195], v[90:93], off
	v_and_b32_e32 v95, 0xffff0000, v184
	v_lshlrev_b32_e32 v96, 16, v185
	v_lshlrev_b32_e32 v90, 16, v182
	v_and_b32_e32 v91, 0xffff0000, v182
	v_and_b32_e32 v97, 0xffff0000, v185
	v_lshlrev_b32_e32 v92, 16, v183
	v_and_b32_e32 v93, 0xffff0000, v183
	v_pk_add_f32 v[86:87], v[86:87], v[90:91]
	v_pk_add_f32 v[90:91], v[84:85], v[96:97]
	v_pk_add_f32 v[84:85], v[82:83], v[94:95]
	v_pk_add_f32 v[88:89], v[88:89], v[92:93]
	v_cvt_pk_bf16_f32 v82, v86, v87
	v_lshlrev_b32_e32 v86, 16, v187
	v_cvt_pk_bf16_f32 v83, v88, v89
	v_cvt_pk_bf16_f32 v84, v84, v85
	v_cvt_pk_bf16_f32 v85, v90, v91
	global_store_dwordx4 v[194:195], v[82:85], off offset:256
	v_and_b32_e32 v87, 0xffff0000, v187
	v_lshlrev_b32_e32 v88, 16, v188
	v_lshlrev_b32_e32 v84, 16, v186
	v_and_b32_e32 v85, 0xffff0000, v186
	v_and_b32_e32 v89, 0xffff0000, v188
	v_lshlrev_b32_e32 v90, 16, v189
	v_and_b32_e32 v91, 0xffff0000, v189
	v_lshl_add_u64 v[82:83], v[144:145], 0, v[196:197]
	v_pk_add_f32 v[80:81], v[80:81], v[86:87]
	v_pk_add_f32 v[78:79], v[78:79], v[84:85]
	v_pk_add_f32 v[84:85], v[76:77], v[90:91]
	v_pk_add_f32 v[76:77], v[74:75], v[88:89]
	v_cvt_pk_bf16_f32 v74, v78, v79
	v_cvt_pk_bf16_f32 v75, v80, v81
	v_lshlrev_b32_e32 v78, 16, v192
	v_cvt_pk_bf16_f32 v76, v76, v77
	v_cvt_pk_bf16_f32 v77, v84, v85
	global_store_dwordx4 v[82:83], v[74:77], off
	v_and_b32_e32 v79, 0xffff0000, v192
	v_lshlrev_b32_e32 v80, 16, v193
	v_lshlrev_b32_e32 v74, 16, v190
	v_and_b32_e32 v75, 0xffff0000, v190
	v_and_b32_e32 v81, 0xffff0000, v193
	v_lshlrev_b32_e32 v76, 16, v191
	v_and_b32_e32 v77, 0xffff0000, v191
	v_pk_add_f32 v[70:71], v[70:71], v[74:75]
	v_pk_add_f32 v[74:75], v[68:69], v[80:81]
	v_pk_add_f32 v[68:69], v[66:67], v[78:79]
	v_pk_add_f32 v[72:73], v[72:73], v[76:77]
	v_cvt_pk_bf16_f32 v66, v70, v71
	s_nop 0
	v_cvt_pk_bf16_f32 v67, v72, v73
	v_cvt_pk_bf16_f32 v68, v68, v69
	v_cvt_pk_bf16_f32 v69, v74, v75
	global_store_dwordx4 v[82:83], v[66:69], off offset:256
	s_waitcnt vmcnt(12)
	v_lshlrev_b32_e32 v86, 16, v226
	v_and_b32_e32 v87, 0xffff0000, v226
	v_lshlrev_b32_e32 v226, 16, v227
	v_and_b32_e32 v227, 0xffff0000, v227
	v_lshlrev_b32_e32 v88, 16, v228
	v_and_b32_e32 v89, 0xffff0000, v228
	v_lshlrev_b32_e32 v228, 16, v229
	v_and_b32_e32 v229, 0xffff0000, v229
	v_lshl_add_u64 v[242:243], v[144:145], 0, v[242:243]
	v_pk_add_f32 v[64:65], v[64:65], v[226:227]
	v_pk_add_f32 v[62:63], v[62:63], v[86:87]
	v_pk_add_f32 v[226:227], v[60:61], v[228:229]
	v_pk_add_f32 v[60:61], v[58:59], v[88:89]
	v_cvt_pk_bf16_f32 v58, v62, v63
	v_cvt_pk_bf16_f32 v59, v64, v65
	v_lshlrev_b32_e32 v62, 16, v232
	v_cvt_pk_bf16_f32 v60, v60, v61
	v_cvt_pk_bf16_f32 v61, v226, v227
	global_store_dwordx4 v[242:243], v[58:61], off
	v_and_b32_e32 v63, 0xffff0000, v232
	v_lshlrev_b32_e32 v64, 16, v233
	v_lshlrev_b32_e32 v58, 16, v230
	v_and_b32_e32 v59, 0xffff0000, v230
	v_and_b32_e32 v65, 0xffff0000, v233
	v_lshlrev_b32_e32 v60, 16, v231
	v_and_b32_e32 v61, 0xffff0000, v231
	v_pk_add_f32 v[54:55], v[54:55], v[58:59]
	v_pk_add_f32 v[58:59], v[52:53], v[64:65]
	v_pk_add_f32 v[52:53], v[50:51], v[62:63]
	v_pk_add_f32 v[56:57], v[56:57], v[60:61]
	v_cvt_pk_bf16_f32 v50, v54, v55
	v_lshlrev_b32_e32 v54, 16, v235
	v_cvt_pk_bf16_f32 v51, v56, v57
	v_cvt_pk_bf16_f32 v52, v52, v53
	v_cvt_pk_bf16_f32 v53, v58, v59
	global_store_dwordx4 v[242:243], v[50:53], off offset:256
	v_and_b32_e32 v55, 0xffff0000, v235
	v_lshlrev_b32_e32 v56, 16, v236
	v_lshlrev_b32_e32 v52, 16, v234
	v_and_b32_e32 v53, 0xffff0000, v234
	v_and_b32_e32 v57, 0xffff0000, v236
	v_lshlrev_b32_e32 v58, 16, v237
	v_and_b32_e32 v59, 0xffff0000, v237
	v_lshl_add_u64 v[50:51], v[144:145], 0, v[244:245]
	v_pk_add_f32 v[48:49], v[48:49], v[54:55]
	v_pk_add_f32 v[46:47], v[46:47], v[52:53]
	v_pk_add_f32 v[52:53], v[44:45], v[58:59]
	v_pk_add_f32 v[44:45], v[42:43], v[56:57]
	v_cvt_pk_bf16_f32 v42, v46, v47
	v_cvt_pk_bf16_f32 v43, v48, v49
	v_lshlrev_b32_e32 v46, 16, v240
	v_cvt_pk_bf16_f32 v44, v44, v45
	v_cvt_pk_bf16_f32 v45, v52, v53
	global_store_dwordx4 v[50:51], v[42:45], off
	v_and_b32_e32 v47, 0xffff0000, v240
	v_lshlrev_b32_e32 v48, 16, v241
	v_lshlrev_b32_e32 v42, 16, v238
	v_and_b32_e32 v43, 0xffff0000, v238
	v_and_b32_e32 v49, 0xffff0000, v241
	v_lshlrev_b32_e32 v44, 16, v239
	v_and_b32_e32 v45, 0xffff0000, v239
	v_pk_add_f32 v[38:39], v[38:39], v[42:43]
	v_pk_add_f32 v[42:43], v[36:37], v[48:49]
	v_pk_add_f32 v[36:37], v[34:35], v[46:47]
	v_pk_add_f32 v[40:41], v[40:41], v[44:45]
	v_cvt_pk_bf16_f32 v34, v38, v39
	s_nop 0
	v_cvt_pk_bf16_f32 v35, v40, v41
	v_cvt_pk_bf16_f32 v36, v36, v37
	v_cvt_pk_bf16_f32 v37, v42, v43
	global_store_dwordx4 v[50:51], v[34:37], off offset:256
	s_waitcnt vmcnt(12)
; #define SB() __builtin_amdgcn_sched_barrier(0)
; __device__ __forceinline__ unsigned cvt_pk_bf16(float lo, float hi) { unsigned r; asm volatile("v_cvt_pk_bf16_f32 %0, %1, %2" : "=v"(r) : "v"(lo), "v"(hi)); return r; }
; __device__ __forceinline__ float bflo(unsigned w) { return __uint_as_float(w << 16); }
; __device__ __forceinline__ float bfhi(unsigned w) { return __uint_as_float(w & 0xffff0000u); }
; #define PG8_BAR __builtin_amdgcn_s_barrier()
;     ...
;         if (!has_next) break;
; #pragma unroll
;         for (int a = 0; a < 2; ++a)
; #pragma unroll
;             for (int b = 0; b < 2; ++b)
; #pragma unroll
;                 for (int m = 0; m < 4; ++m)
; #pragma unroll
;                     for (int n = 0; n < 2; ++n) acc[a][b][m][n] = (f32x4){0.f, 0.f, 0.f, 0.f};
;         cur = nxt; cA = nA; cB = nB; ++ui; nt = PG8_NT(cur);
;         if constexpr (GATHER) { cg[0] = ng[0]; cg[1] = ng[1]; }
;         if constexpr (ALIGN_EPI) { if (wr == 1) PG8_BAR; }
;     __device__ __forceinline__ void operator()(const f32x4 (&acc)[2][2][4][2], const Unit& u, int wr, int wc, int fr, int fq) const {
;     ...
;             for (int mm = 0; mm < 2; ++mm) { const int m = mh + mm; const size_t ro = (size_t)(ai * HALF + wr * 64 + m * 16 + fr) * u.ldc;
; #pragma unroll
;                 for (int bj = 0; bj < 2; ++bj) { f32x4 r0, r1;
;                     if constexpr (RF32) { r0 = rv[mm][bj][0]; r1 = rv[mm][bj][1]; }
;                     else { const u32x4 q = rw[mm][bj]; r0 = f32x4{bflo(q.x), bfhi(q.x), bflo(q.y), bfhi(q.y)}; r1 = f32x4{bflo(q.z), bfhi(q.z), bflo(q.w), bfhi(q.w)}; }
;                     const f32x4 v0 = acc[ai][bj][m][0] + r0, v1 = acc[ai][bj][m][1] + r1;
;                     u32x4 w; w.x = cvt_pk_bf16(v0[0], v0[1]); w.y = cvt_pk_bf16(v0[2], v0[3]); w.z = cvt_pk_bf16(v1[0], v1[1]); w.w = cvt_pk_bf16(v1[2], v1[3]);
;                     *(u32x4*)(cb + ro + bj * HALF) = w; } }
;             SB(); } }
	v_lshlrev_b32_e32 v54, 16, v198
	v_and_b32_e32 v55, 0xffff0000, v198
	v_lshlrev_b32_e32 v198, 16, v199
	v_and_b32_e32 v199, 0xffff0000, v199
	v_lshlrev_b32_e32 v56, 16, v200
	v_and_b32_e32 v57, 0xffff0000, v200
	v_lshlrev_b32_e32 v200, 16, v201
	v_and_b32_e32 v201, 0xffff0000, v201
	v_lshl_add_u64 v[214:215], v[144:145], 0, v[214:215]
	v_pk_add_f32 v[32:33], v[32:33], v[198:199]
	v_pk_add_f32 v[30:31], v[30:31], v[54:55]
	v_pk_add_f32 v[198:199], v[28:29], v[200:201]
	v_pk_add_f32 v[28:29], v[26:27], v[56:57]
	v_cvt_pk_bf16_f32 v26, v30, v31
	v_cvt_pk_bf16_f32 v27, v32, v33
	v_lshlrev_b32_e32 v30, 16, v204
	v_cvt_pk_bf16_f32 v28, v28, v29
	v_cvt_pk_bf16_f32 v29, v198, v199
	global_store_dwordx4 v[214:215], v[26:29], off
	v_and_b32_e32 v31, 0xffff0000, v204
	v_lshlrev_b32_e32 v32, 16, v205
	v_lshlrev_b32_e32 v26, 16, v202
	v_and_b32_e32 v27, 0xffff0000, v202
	v_and_b32_e32 v33, 0xffff0000, v205
	v_lshlrev_b32_e32 v28, 16, v203
	v_and_b32_e32 v29, 0xffff0000, v203
	v_pk_add_f32 v[22:23], v[22:23], v[26:27]
	v_pk_add_f32 v[26:27], v[20:21], v[32:33]
	v_pk_add_f32 v[20:21], v[18:19], v[30:31]
	v_pk_add_f32 v[24:25], v[24:25], v[28:29]
	v_cvt_pk_bf16_f32 v18, v22, v23
	v_lshlrev_b32_e32 v22, 16, v207
	v_cvt_pk_bf16_f32 v19, v24, v25
	v_cvt_pk_bf16_f32 v20, v20, v21
	v_cvt_pk_bf16_f32 v21, v26, v27
	global_store_dwordx4 v[214:215], v[18:21], off offset:256
	v_and_b32_e32 v23, 0xffff0000, v207
	v_lshlrev_b32_e32 v24, 16, v208
	v_lshlrev_b32_e32 v20, 16, v206
	v_and_b32_e32 v21, 0xffff0000, v206
	v_and_b32_e32 v25, 0xffff0000, v208
	v_lshlrev_b32_e32 v26, 16, v209
	v_and_b32_e32 v27, 0xffff0000, v209
	v_lshl_add_u64 v[18:19], v[144:145], 0, v[246:247]
	v_pk_add_f32 v[16:17], v[16:17], v[22:23]
	v_pk_add_f32 v[14:15], v[14:15], v[20:21]
	v_pk_add_f32 v[20:21], v[12:13], v[26:27]
	v_pk_add_f32 v[12:13], v[10:11], v[24:25]
	v_cvt_pk_bf16_f32 v10, v14, v15
	v_cvt_pk_bf16_f32 v11, v16, v17
	v_lshlrev_b32_e32 v14, 16, v212
	v_cvt_pk_bf16_f32 v12, v12, v13
	v_cvt_pk_bf16_f32 v13, v20, v21
	global_store_dwordx4 v[18:19], v[10:13], off
	v_and_b32_e32 v15, 0xffff0000, v212
	v_lshlrev_b32_e32 v16, 16, v213
	v_lshlrev_b32_e32 v10, 16, v210
	v_and_b32_e32 v11, 0xffff0000, v210
	v_and_b32_e32 v17, 0xffff0000, v213
	v_lshlrev_b32_e32 v12, 16, v211
	v_and_b32_e32 v13, 0xffff0000, v211
	v_pk_add_f32 v[6:7], v[6:7], v[10:11]
	v_pk_add_f32 v[10:11], v[4:5], v[16:17]
	v_pk_add_f32 v[4:5], v[2:3], v[14:15]
	v_pk_add_f32 v[8:9], v[8:9], v[12:13]
	v_cvt_pk_bf16_f32 v2, v6, v7
	s_nop 0
	v_cvt_pk_bf16_f32 v3, v8, v9
	v_cvt_pk_bf16_f32 v4, v4, v5
	v_cvt_pk_bf16_f32 v5, v10, v11
	global_store_dwordx4 v[18:19], v[2:5], off offset:256
	v_readlane_b32 s20, v248, 15
	v_readlane_b32 s22, v248, 19
	s_andn2_b64 vcc, exec, s[36:37]
	s_mov_b64 s[36:37], -1
	v_readlane_b32 s21, v248, 16
	v_readlane_b32 s23, v248, 20
	s_cbranch_vccnz .LBB0_1384
	s_and_b64 vcc, exec, s[56:57]
	s_cbranch_vccnz .LBB0_1383
	s_barrier
	s_branch .LBB0_1383
